# x14v3: one polling wave per consumer workgroup (LDS copy of the progress words), wave-0 vmcnt(17)
# speedup vs baseline: 1.0345x; 1.0345x over previous
.LBB0_1725:
	s_cmp_eq_u32 s82, 0
	s_cbranch_scc1 .Lx14_w0
	s_waitcnt vmcnt(16)
	s_branch .Lx14_wj
.Lx14_w0:
	s_waitcnt vmcnt(17)

.Lx14_sb_done:
	s_or_b64 exec, exec, s[98:99]
	s_barrier
	v_mbcnt_lo_u32_b32 v1, -1, 0
	v_mbcnt_hi_u32_b32 v1, -1, v1
	v_lshlrev_b32_e32 v9, 2, v1
	v_mov_b32_e32 v5, 0
	s_cmp_lg_u32 s82, 0
	s_cbranch_scc1 .Lx14_linit
	ds_write_b32 v9, v5
	ds_write_b32 v9, v5 offset:256
	ds_write_b32 v9, v5 offset:512
	s_waitcnt lgkmcnt(0)
.Lx14_linit:
	s_barrier
	v_mbcnt_lo_u32_b32 v1, -1, 0
	v_mbcnt_hi_u32_b32 v1, -1, v1
	v_lshlrev_b32_e32 v2, 4, v1
	v_lshrrev_b32_e32 v3, 3, v1
	v_lshlrev_b32_e32 v3, 2, v3
	v_and_b32_e32 v4, 31, v1
	v_lshlrev_b32_e32 v4, 2, v4
	v_lshrrev_b32_e32 v9, 5, v1
	v_lshl_add_u32 v4, v9, 8, v4
	v_lshlrev_b32_e32 v9, 5, v1
	s_load_dwordx4 s[28:31], s[74:75], 0x100
	s_add_u32 s4, s54, 0x8c00000
	s_addc_u32 s5, s55, 0
	s_add_u32 s6, s54, 0x29400000
	s_addc_u32 s7, s55, 0
	s_add_u32 s8, s54, 0x21200000
	s_addc_u32 s9, s55, 0
	s_add_u32 s10, s54, 0x49c00000
	s_addc_u32 s11, s55, 0
	s_add_u32 s12, s54, 0x19000000
	s_addc_u32 s13, s55, 0
	s_add_u32 s14, s54, 0xc00000
	s_addc_u32 s15, s55, 0
	s_add_u32 s16, s54, 0x1000000
	s_addc_u32 s17, s55, 0
	s_add_u32 s20, s54, 0xc400
	s_addc_u32 s21, s55, 0
	s_mov_b32 s18, -1
	s_mov_b32 s19, 0
	s_add_i32 s25, s2, 0xffffff80
	s_lshl_b32 s25, s25, 3
	s_add_i32 s25, s25, s82
	s_lshr_b32 s100, s25, 8
	s_and_b32 s25, s25, 0xff
	s_mov_b32 s24, 0
	s_mov_b32 s26, 0
	s_waitcnt lgkmcnt(0)
	global_load_dwordx4 v[10:13], v9, s[28:29]
	global_load_dwordx4 v[14:17], v9, s[28:29] offset:16
	global_load_dwordx4 v[18:21], v9, s[28:29] offset:2048
	global_load_dwordx4 v[22:25], v9, s[28:29] offset:2064
	global_load_dwordx4 v[42:45], v9, s[30:31]
	global_load_dwordx4 v[46:49], v9, s[30:31] offset:16
	global_load_dwordx4 v[50:53], v9, s[30:31] offset:2048
	global_load_dwordx4 v[54:57], v9, s[30:31] offset:2064
	v_add_u32_e32 v9, 0x1000, v9
	global_load_dwordx4 v[26:29], v9, s[28:29]
	global_load_dwordx4 v[30:33], v9, s[28:29] offset:16
	global_load_dwordx4 v[34:37], v9, s[28:29] offset:2048
	global_load_dwordx4 v[38:41], v9, s[28:29] offset:2064
	global_load_dwordx4 v[58:61], v9, s[30:31]
	global_load_dwordx4 v[62:65], v9, s[30:31] offset:16
	global_load_dwordx4 v[66:69], v9, s[30:31] offset:2048
	global_load_dwordx4 v[70:73], v9, s[30:31] offset:2064
	s_waitcnt vmcnt(0)

.Lx14_poll:
	s_cmp_lg_u32 s82, 0
	s_cbranch_scc1 .Lx14_test
	global_load_dword v9, v4, s[20:21] sc1
	global_load_dword v152, v4, s[20:21] offset:128 sc1
	s_waitcnt vmcnt(0)
	ds_write_b32 v4, v9
	ds_write_b32 v4, v152 offset:128
	s_waitcnt lgkmcnt(0)
.Lx14_test:
	ds_read_b32 v9, v7
	s_waitcnt lgkmcnt(0)
	v_cmp_lt_i32_e32 vcc, v9, v8
	s_cbranch_vccz .Lx14_ready
	s_sleep 32
	s_add_u32 s27, s27, 1
	s_cmp_lt_u32 s27, 0x4000
	s_cbranch_scc1 .Lx14_poll
	s_mov_b32 s26, 1
.Lx14_ready:
	global_load_dwordx4 v[80:83], v5, s[4:5] sc1
	global_load_dwordx4 v[84:87], v5, s[4:5] offset:1024 sc1
	global_load_dwordx4 v[88:91], v5, s[4:5] offset:2048 sc1
	global_load_dwordx4 v[92:95], v5, s[4:5] offset:3072 sc1
	global_load_dwordx4 v[96:99], v5, s[6:7] sc1
	global_load_dwordx4 v[100:103], v5, s[6:7] offset:1024 sc1
	global_load_dwordx4 v[104:107], v5, s[6:7] offset:2048 sc1
	global_load_dwordx4 v[108:111], v5, s[6:7] offset:3072 sc1
	s_waitcnt vmcnt(0)
	v_lshlrev_b32_e32 v168, 16, v80
	v_lshlrev_b32_e32 v169, 16, v96
	v_add_f32_e32 v160, v168, v169
	v_and_b32_e32 v168, 0xffff0000, v80
	v_and_b32_e32 v169, 0xffff0000, v96
	v_add_f32_e32 v161, v168, v169
	v_lshlrev_b32_e32 v168, 16, v81
	v_lshlrev_b32_e32 v169, 16, v97
	v_add_f32_e32 v162, v168, v169
	v_and_b32_e32 v168, 0xffff0000, v81
	v_and_b32_e32 v169, 0xffff0000, v97
	v_add_f32_e32 v163, v168, v169
	v_lshlrev_b32_e32 v168, 16, v82
	v_lshlrev_b32_e32 v169, 16, v98
	v_add_f32_e32 v164, v168, v169
	v_and_b32_e32 v168, 0xffff0000, v82
	v_and_b32_e32 v169, 0xffff0000, v98
	v_add_f32_e32 v165, v168, v169
	v_lshlrev_b32_e32 v168, 16, v83
	v_lshlrev_b32_e32 v169, 16, v99
	v_add_f32_e32 v166, v168, v169
	v_and_b32_e32 v168, 0xffff0000, v83
	v_and_b32_e32 v169, 0xffff0000, v99
	v_add_f32_e32 v167, v168, v169
	v_add_f32_e32 v170, v160, v161
	v_add_f32_e32 v170, v170, v162
	v_add_f32_e32 v170, v170, v163
	v_add_f32_e32 v170, v170, v164
	v_add_f32_e32 v170, v170, v165
	v_add_f32_e32 v170, v170, v166
	v_add_f32_e32 v170, v170, v167
	s_nop 1
	v_add_f32_dpp v170, v170, v170 quad_perm:[1,0,3,2] row_mask:0xf bank_mask:0xf bound_ctrl:1
	s_nop 1
	v_add_f32_dpp v170, v170, v170 quad_perm:[2,3,0,1] row_mask:0xf bank_mask:0xf bound_ctrl:1
	s_nop 1
	v_add_f32_dpp v170, v170, v170 row_half_mirror row_mask:0xf bank_mask:0xf bound_ctrl:1
	v_mul_f32_e32 v170, 0x3c800000, v170
	v_sub_f32_e32 v160, v160, v170
	v_sub_f32_e32 v161, v161, v170
	v_sub_f32_e32 v162, v162, v170
	v_sub_f32_e32 v163, v163, v170
	v_sub_f32_e32 v164, v164, v170
	v_sub_f32_e32 v165, v165, v170
	v_sub_f32_e32 v166, v166, v170
	v_sub_f32_e32 v167, v167, v170
	v_mul_f32_e32 v171, v160, v160
	v_fmac_f32_e32 v171, v161, v161
	v_fmac_f32_e32 v171, v162, v162
	v_fmac_f32_e32 v171, v163, v163
	v_fmac_f32_e32 v171, v164, v164
	v_fmac_f32_e32 v171, v165, v165
	v_fmac_f32_e32 v171, v166, v166
	v_fmac_f32_e32 v171, v167, v167
	s_nop 1
	v_add_f32_dpp v171, v171, v171 quad_perm:[1,0,3,2] row_mask:0xf bank_mask:0xf bound_ctrl:1
	s_nop 1
	v_add_f32_dpp v171, v171, v171 quad_perm:[2,3,0,1] row_mask:0xf bank_mask:0xf bound_ctrl:1
	s_nop 1
	v_add_f32_dpp v171, v171, v171 row_half_mirror row_mask:0xf bank_mask:0xf bound_ctrl:1
	v_mov_b32_e32 v172, 0x3a27c5ac
	v_fmac_f32_e32 v172, 0x3c800000, v171
	v_rsq_f32_e32 v172, v172
	v_add_f32_e32 v173, v144, v148
	s_nop 0
	v_mul_f32_e32 v160, v160, v172
	v_mul_f32_e32 v161, v161, v172
	v_mul_f32_e32 v162, v162, v172
	v_mul_f32_e32 v163, v163, v172
	v_mul_f32_e32 v164, v164, v172
	v_mul_f32_e32 v165, v165, v172
	v_mul_f32_e32 v166, v166, v172
	v_mul_f32_e32 v167, v167, v172
	v_fma_f32 v160, v10, v160, v42
	v_fma_f32 v161, v11, v161, v43
	v_fma_f32 v162, v12, v162, v44
	v_fma_f32 v163, v13, v163, v45
	v_fma_f32 v164, v14, v164, v46
	v_fma_f32 v165, v15, v165, v47
	v_fma_f32 v166, v16, v166, v48
	v_fma_f32 v167, v17, v167, v49
	v_lshlrev_b32_e32 v168, 16, v112
	v_fmac_f32_e32 v160, v173, v168
	v_and_b32_e32 v169, 0xffff0000, v112
	v_fmac_f32_e32 v161, v173, v169
	v_lshlrev_b32_e32 v168, 16, v128
	v_mul_f32_e32 v160, v160, v168
	v_and_b32_e32 v169, 0xffff0000, v128
	v_mul_f32_e32 v161, v161, v169
	v_lshlrev_b32_e32 v168, 16, v113
	v_fmac_f32_e32 v162, v173, v168
	v_and_b32_e32 v169, 0xffff0000, v113
	v_fmac_f32_e32 v163, v173, v169
	v_lshlrev_b32_e32 v168, 16, v129
	v_mul_f32_e32 v162, v162, v168
	v_and_b32_e32 v169, 0xffff0000, v129
	v_mul_f32_e32 v163, v163, v169
	v_lshlrev_b32_e32 v168, 16, v114
	v_fmac_f32_e32 v164, v173, v168
	v_and_b32_e32 v169, 0xffff0000, v114
	v_fmac_f32_e32 v165, v173, v169
	v_lshlrev_b32_e32 v168, 16, v130
	v_mul_f32_e32 v164, v164, v168
	v_and_b32_e32 v169, 0xffff0000, v130
	v_mul_f32_e32 v165, v165, v169
	v_lshlrev_b32_e32 v168, 16, v115
	v_fmac_f32_e32 v166, v173, v168
	v_and_b32_e32 v169, 0xffff0000, v115
	v_fmac_f32_e32 v167, v173, v169
	v_lshlrev_b32_e32 v168, 16, v131
	v_mul_f32_e32 v166, v166, v168
	v_and_b32_e32 v169, 0xffff0000, v131
	v_mul_f32_e32 v167, v167, v169
	v_cvt_pk_bf16_f32 v180, v160, v161
	v_cvt_pk_bf16_f32 v181, v162, v163
	v_cvt_pk_bf16_f32 v182, v164, v165
	v_cvt_pk_bf16_f32 v183, v166, v167
	global_store_dwordx4 v5, v[180:183], s[12:13]
	v_lshlrev_b32_e32 v168, 16, v84
	v_lshlrev_b32_e32 v169, 16, v100
	v_add_f32_e32 v160, v168, v169
	v_and_b32_e32 v168, 0xffff0000, v84
	v_and_b32_e32 v169, 0xffff0000, v100
	v_add_f32_e32 v161, v168, v169
	v_lshlrev_b32_e32 v168, 16, v85
	v_lshlrev_b32_e32 v169, 16, v101
	v_add_f32_e32 v162, v168, v169
	v_and_b32_e32 v168, 0xffff0000, v85
	v_and_b32_e32 v169, 0xffff0000, v101
	v_add_f32_e32 v163, v168, v169
	v_lshlrev_b32_e32 v168, 16, v86
	v_lshlrev_b32_e32 v169, 16, v102
	v_add_f32_e32 v164, v168, v169
	v_and_b32_e32 v168, 0xffff0000, v86
	v_and_b32_e32 v169, 0xffff0000, v102
	v_add_f32_e32 v165, v168, v169
	v_lshlrev_b32_e32 v168, 16, v87
	v_lshlrev_b32_e32 v169, 16, v103
	v_add_f32_e32 v166, v168, v169
	v_and_b32_e32 v168, 0xffff0000, v87
	v_and_b32_e32 v169, 0xffff0000, v103
	v_add_f32_e32 v167, v168, v169
	v_add_f32_e32 v170, v160, v161
	v_add_f32_e32 v170, v170, v162
	v_add_f32_e32 v170, v170, v163
	v_add_f32_e32 v170, v170, v164
	v_add_f32_e32 v170, v170, v165
	v_add_f32_e32 v170, v170, v166
	v_add_f32_e32 v170, v170, v167
	s_nop 1
	v_add_f32_dpp v170, v170, v170 quad_perm:[1,0,3,2] row_mask:0xf bank_mask:0xf bound_ctrl:1
	s_nop 1
	v_add_f32_dpp v170, v170, v170 quad_perm:[2,3,0,1] row_mask:0xf bank_mask:0xf bound_ctrl:1
	s_nop 1
	v_add_f32_dpp v170, v170, v170 row_half_mirror row_mask:0xf bank_mask:0xf bound_ctrl:1
	v_mul_f32_e32 v170, 0x3c800000, v170
	v_sub_f32_e32 v160, v160, v170
	v_sub_f32_e32 v161, v161, v170
	v_sub_f32_e32 v162, v162, v170
	v_sub_f32_e32 v163, v163, v170
	v_sub_f32_e32 v164, v164, v170
	v_sub_f32_e32 v165, v165, v170
	v_sub_f32_e32 v166, v166, v170
	v_sub_f32_e32 v167, v167, v170
	v_mul_f32_e32 v171, v160, v160
	v_fmac_f32_e32 v171, v161, v161
	v_fmac_f32_e32 v171, v162, v162
	v_fmac_f32_e32 v171, v163, v163
	v_fmac_f32_e32 v171, v164, v164
	v_fmac_f32_e32 v171, v165, v165
	v_fmac_f32_e32 v171, v166, v166
	v_fmac_f32_e32 v171, v167, v167
	s_nop 1
	v_add_f32_dpp v171, v171, v171 quad_perm:[1,0,3,2] row_mask:0xf bank_mask:0xf bound_ctrl:1
	s_nop 1
	v_add_f32_dpp v171, v171, v171 quad_perm:[2,3,0,1] row_mask:0xf bank_mask:0xf bound_ctrl:1
	s_nop 1
	v_add_f32_dpp v171, v171, v171 row_half_mirror row_mask:0xf bank_mask:0xf bound_ctrl:1
	v_mov_b32_e32 v172, 0x3a27c5ac
	v_fmac_f32_e32 v172, 0x3c800000, v171
	v_rsq_f32_e32 v172, v172
	v_add_f32_e32 v173, v145, v149
	s_nop 0
	v_mul_f32_e32 v160, v160, v172
	v_mul_f32_e32 v161, v161, v172
	v_mul_f32_e32 v162, v162, v172
	v_mul_f32_e32 v163, v163, v172
	v_mul_f32_e32 v164, v164, v172
	v_mul_f32_e32 v165, v165, v172
	v_mul_f32_e32 v166, v166, v172
	v_mul_f32_e32 v167, v167, v172
	v_fma_f32 v160, v18, v160, v50
	v_fma_f32 v161, v19, v161, v51
	v_fma_f32 v162, v20, v162, v52
	v_fma_f32 v163, v21, v163, v53
	v_fma_f32 v164, v22, v164, v54
	v_fma_f32 v165, v23, v165, v55
	v_fma_f32 v166, v24, v166, v56
	v_fma_f32 v167, v25, v167, v57
	v_lshlrev_b32_e32 v168, 16, v116
	v_fmac_f32_e32 v160, v173, v168
	v_and_b32_e32 v169, 0xffff0000, v116
	v_fmac_f32_e32 v161, v173, v169
	v_lshlrev_b32_e32 v168, 16, v132
	v_mul_f32_e32 v160, v160, v168
	v_and_b32_e32 v169, 0xffff0000, v132
	v_mul_f32_e32 v161, v161, v169
	v_lshlrev_b32_e32 v168, 16, v117
	v_fmac_f32_e32 v162, v173, v168
	v_and_b32_e32 v169, 0xffff0000, v117
	v_fmac_f32_e32 v163, v173, v169
	v_lshlrev_b32_e32 v168, 16, v133
	v_mul_f32_e32 v162, v162, v168
	v_and_b32_e32 v169, 0xffff0000, v133
	v_mul_f32_e32 v163, v163, v169
	v_lshlrev_b32_e32 v168, 16, v118
	v_fmac_f32_e32 v164, v173, v168
	v_and_b32_e32 v169, 0xffff0000, v118
	v_fmac_f32_e32 v165, v173, v169
	v_lshlrev_b32_e32 v168, 16, v134
	v_mul_f32_e32 v164, v164, v168
	v_and_b32_e32 v169, 0xffff0000, v134
	v_mul_f32_e32 v165, v165, v169
	v_lshlrev_b32_e32 v168, 16, v119
	v_fmac_f32_e32 v166, v173, v168
	v_and_b32_e32 v169, 0xffff0000, v119
	v_fmac_f32_e32 v167, v173, v169
	v_lshlrev_b32_e32 v168, 16, v135
	v_mul_f32_e32 v166, v166, v168
	v_and_b32_e32 v169, 0xffff0000, v135
	v_mul_f32_e32 v167, v167, v169
	v_cvt_pk_bf16_f32 v184, v160, v161
	v_cvt_pk_bf16_f32 v185, v162, v163
	v_cvt_pk_bf16_f32 v186, v164, v165
	v_cvt_pk_bf16_f32 v187, v166, v167
	global_store_dwordx4 v5, v[184:187], s[12:13] offset:1024
	v_lshlrev_b32_e32 v168, 16, v88
	v_lshlrev_b32_e32 v169, 16, v104
	v_add_f32_e32 v160, v168, v169
	v_and_b32_e32 v168, 0xffff0000, v88
	v_and_b32_e32 v169, 0xffff0000, v104
	v_add_f32_e32 v161, v168, v169
	v_lshlrev_b32_e32 v168, 16, v89
	v_lshlrev_b32_e32 v169, 16, v105
	v_add_f32_e32 v162, v168, v169
	v_and_b32_e32 v168, 0xffff0000, v89
	v_and_b32_e32 v169, 0xffff0000, v105
	v_add_f32_e32 v163, v168, v169
	v_lshlrev_b32_e32 v168, 16, v90
	v_lshlrev_b32_e32 v169, 16, v106
	v_add_f32_e32 v164, v168, v169
	v_and_b32_e32 v168, 0xffff0000, v90
	v_and_b32_e32 v169, 0xffff0000, v106
	v_add_f32_e32 v165, v168, v169
	v_lshlrev_b32_e32 v168, 16, v91
	v_lshlrev_b32_e32 v169, 16, v107
	v_add_f32_e32 v166, v168, v169
	v_and_b32_e32 v168, 0xffff0000, v91
	v_and_b32_e32 v169, 0xffff0000, v107
	v_add_f32_e32 v167, v168, v169
	v_add_f32_e32 v170, v160, v161
	v_add_f32_e32 v170, v170, v162
	v_add_f32_e32 v170, v170, v163
	v_add_f32_e32 v170, v170, v164
	v_add_f32_e32 v170, v170, v165
	v_add_f32_e32 v170, v170, v166
	v_add_f32_e32 v170, v170, v167
	s_nop 1
	v_add_f32_dpp v170, v170, v170 quad_perm:[1,0,3,2] row_mask:0xf bank_mask:0xf bound_ctrl:1
	s_nop 1
	v_add_f32_dpp v170, v170, v170 quad_perm:[2,3,0,1] row_mask:0xf bank_mask:0xf bound_ctrl:1
	s_nop 1
	v_add_f32_dpp v170, v170, v170 row_half_mirror row_mask:0xf bank_mask:0xf bound_ctrl:1
	v_mul_f32_e32 v170, 0x3c800000, v170
	v_sub_f32_e32 v160, v160, v170
	v_sub_f32_e32 v161, v161, v170
	v_sub_f32_e32 v162, v162, v170
	v_sub_f32_e32 v163, v163, v170
	v_sub_f32_e32 v164, v164, v170
	v_sub_f32_e32 v165, v165, v170
	v_sub_f32_e32 v166, v166, v170
	v_sub_f32_e32 v167, v167, v170
	v_mul_f32_e32 v171, v160, v160
	v_fmac_f32_e32 v171, v161, v161
	v_fmac_f32_e32 v171, v162, v162
	v_fmac_f32_e32 v171, v163, v163
	v_fmac_f32_e32 v171, v164, v164
	v_fmac_f32_e32 v171, v165, v165
	v_fmac_f32_e32 v171, v166, v166
	v_fmac_f32_e32 v171, v167, v167
	s_nop 1
	v_add_f32_dpp v171, v171, v171 quad_perm:[1,0,3,2] row_mask:0xf bank_mask:0xf bound_ctrl:1
	s_nop 1
	v_add_f32_dpp v171, v171, v171 quad_perm:[2,3,0,1] row_mask:0xf bank_mask:0xf bound_ctrl:1
	s_nop 1
	v_add_f32_dpp v171, v171, v171 row_half_mirror row_mask:0xf bank_mask:0xf bound_ctrl:1
	v_mov_b32_e32 v172, 0x3a27c5ac
	v_fmac_f32_e32 v172, 0x3c800000, v171
	v_rsq_f32_e32 v172, v172
	v_add_f32_e32 v173, v146, v150
	s_nop 0
	v_mul_f32_e32 v160, v160, v172
	v_mul_f32_e32 v161, v161, v172
	v_mul_f32_e32 v162, v162, v172
	v_mul_f32_e32 v163, v163, v172
	v_mul_f32_e32 v164, v164, v172
	v_mul_f32_e32 v165, v165, v172
	v_mul_f32_e32 v166, v166, v172
	v_mul_f32_e32 v167, v167, v172
	v_fma_f32 v160, v26, v160, v58
	v_fma_f32 v161, v27, v161, v59
	v_fma_f32 v162, v28, v162, v60
	v_fma_f32 v163, v29, v163, v61
	v_fma_f32 v164, v30, v164, v62
	v_fma_f32 v165, v31, v165, v63
	v_fma_f32 v166, v32, v166, v64
	v_fma_f32 v167, v33, v167, v65
	v_lshlrev_b32_e32 v168, 16, v120
	v_fmac_f32_e32 v160, v173, v168
	v_and_b32_e32 v169, 0xffff0000, v120
	v_fmac_f32_e32 v161, v173, v169
	v_lshlrev_b32_e32 v168, 16, v136
	v_mul_f32_e32 v160, v160, v168
	v_and_b32_e32 v169, 0xffff0000, v136
	v_mul_f32_e32 v161, v161, v169
	v_lshlrev_b32_e32 v168, 16, v121
	v_fmac_f32_e32 v162, v173, v168
	v_and_b32_e32 v169, 0xffff0000, v121
	v_fmac_f32_e32 v163, v173, v169
	v_lshlrev_b32_e32 v168, 16, v137
	v_mul_f32_e32 v162, v162, v168
	v_and_b32_e32 v169, 0xffff0000, v137
	v_mul_f32_e32 v163, v163, v169
	v_lshlrev_b32_e32 v168, 16, v122
	v_fmac_f32_e32 v164, v173, v168
	v_and_b32_e32 v169, 0xffff0000, v122
	v_fmac_f32_e32 v165, v173, v169
	v_lshlrev_b32_e32 v168, 16, v138
	v_mul_f32_e32 v164, v164, v168
	v_and_b32_e32 v169, 0xffff0000, v138
	v_mul_f32_e32 v165, v165, v169
	v_lshlrev_b32_e32 v168, 16, v123
	v_fmac_f32_e32 v166, v173, v168
	v_and_b32_e32 v169, 0xffff0000, v123
	v_fmac_f32_e32 v167, v173, v169
	v_lshlrev_b32_e32 v168, 16, v139
	v_mul_f32_e32 v166, v166, v168
	v_and_b32_e32 v169, 0xffff0000, v139
	v_mul_f32_e32 v167, v167, v169
	v_cvt_pk_bf16_f32 v192, v160, v161
	v_cvt_pk_bf16_f32 v193, v162, v163
	v_cvt_pk_bf16_f32 v194, v164, v165
	v_cvt_pk_bf16_f32 v195, v166, v167
	global_store_dwordx4 v5, v[192:195], s[12:13] offset:2048
	v_lshlrev_b32_e32 v168, 16, v92
	v_lshlrev_b32_e32 v169, 16, v108
	v_add_f32_e32 v160, v168, v169
	v_and_b32_e32 v168, 0xffff0000, v92
	v_and_b32_e32 v169, 0xffff0000, v108
	v_add_f32_e32 v161, v168, v169
	v_lshlrev_b32_e32 v168, 16, v93
	v_lshlrev_b32_e32 v169, 16, v109
	v_add_f32_e32 v162, v168, v169
	v_and_b32_e32 v168, 0xffff0000, v93
	v_and_b32_e32 v169, 0xffff0000, v109
	v_add_f32_e32 v163, v168, v169
	v_lshlrev_b32_e32 v168, 16, v94
	v_lshlrev_b32_e32 v169, 16, v110
	v_add_f32_e32 v164, v168, v169
	v_and_b32_e32 v168, 0xffff0000, v94
	v_and_b32_e32 v169, 0xffff0000, v110
	v_add_f32_e32 v165, v168, v169
	v_lshlrev_b32_e32 v168, 16, v95
	v_lshlrev_b32_e32 v169, 16, v111
	v_add_f32_e32 v166, v168, v169
	v_and_b32_e32 v168, 0xffff0000, v95
	v_and_b32_e32 v169, 0xffff0000, v111
	v_add_f32_e32 v167, v168, v169
	v_add_f32_e32 v170, v160, v161
	v_add_f32_e32 v170, v170, v162
	v_add_f32_e32 v170, v170, v163
	v_add_f32_e32 v170, v170, v164
	v_add_f32_e32 v170, v170, v165
	v_add_f32_e32 v170, v170, v166
	v_add_f32_e32 v170, v170, v167
	s_nop 1
	v_add_f32_dpp v170, v170, v170 quad_perm:[1,0,3,2] row_mask:0xf bank_mask:0xf bound_ctrl:1
	s_nop 1
	v_add_f32_dpp v170, v170, v170 quad_perm:[2,3,0,1] row_mask:0xf bank_mask:0xf bound_ctrl:1
	s_nop 1
	v_add_f32_dpp v170, v170, v170 row_half_mirror row_mask:0xf bank_mask:0xf bound_ctrl:1
	v_mul_f32_e32 v170, 0x3c800000, v170
	v_sub_f32_e32 v160, v160, v170
	v_sub_f32_e32 v161, v161, v170
	v_sub_f32_e32 v162, v162, v170
	v_sub_f32_e32 v163, v163, v170
	v_sub_f32_e32 v164, v164, v170
	v_sub_f32_e32 v165, v165, v170
	v_sub_f32_e32 v166, v166, v170
	v_sub_f32_e32 v167, v167, v170
	v_mul_f32_e32 v171, v160, v160
	v_fmac_f32_e32 v171, v161, v161
	v_fmac_f32_e32 v171, v162, v162
	v_fmac_f32_e32 v171, v163, v163
	v_fmac_f32_e32 v171, v164, v164
	v_fmac_f32_e32 v171, v165, v165
	v_fmac_f32_e32 v171, v166, v166
	v_fmac_f32_e32 v171, v167, v167
	s_nop 1
	v_add_f32_dpp v171, v171, v171 quad_perm:[1,0,3,2] row_mask:0xf bank_mask:0xf bound_ctrl:1
	s_nop 1
	v_add_f32_dpp v171, v171, v171 quad_perm:[2,3,0,1] row_mask:0xf bank_mask:0xf bound_ctrl:1
	s_nop 1
	v_add_f32_dpp v171, v171, v171 row_half_mirror row_mask:0xf bank_mask:0xf bound_ctrl:1
	v_mov_b32_e32 v172, 0x3a27c5ac
	v_fmac_f32_e32 v172, 0x3c800000, v171
	v_rsq_f32_e32 v172, v172
	v_add_f32_e32 v173, v147, v151
	s_nop 0
	v_mul_f32_e32 v160, v160, v172
	v_mul_f32_e32 v161, v161, v172
	v_mul_f32_e32 v162, v162, v172
	v_mul_f32_e32 v163, v163, v172
	v_mul_f32_e32 v164, v164, v172
	v_mul_f32_e32 v165, v165, v172
	v_mul_f32_e32 v166, v166, v172
	v_mul_f32_e32 v167, v167, v172
	v_fma_f32 v160, v34, v160, v66
	v_fma_f32 v161, v35, v161, v67
	v_fma_f32 v162, v36, v162, v68
	v_fma_f32 v163, v37, v163, v69
	v_fma_f32 v164, v38, v164, v70
	v_fma_f32 v165, v39, v165, v71
	v_fma_f32 v166, v40, v166, v72
	v_fma_f32 v167, v41, v167, v73
	v_lshlrev_b32_e32 v168, 16, v124
	v_fmac_f32_e32 v160, v173, v168
	v_and_b32_e32 v169, 0xffff0000, v124
	v_fmac_f32_e32 v161, v173, v169
	v_lshlrev_b32_e32 v168, 16, v140
	v_mul_f32_e32 v160, v160, v168
	v_and_b32_e32 v169, 0xffff0000, v140
	v_mul_f32_e32 v161, v161, v169
	v_lshlrev_b32_e32 v168, 16, v125
	v_fmac_f32_e32 v162, v173, v168
	v_and_b32_e32 v169, 0xffff0000, v125
	v_fmac_f32_e32 v163, v173, v169
	v_lshlrev_b32_e32 v168, 16, v141
	v_mul_f32_e32 v162, v162, v168
	v_and_b32_e32 v169, 0xffff0000, v141
	v_mul_f32_e32 v163, v163, v169
	v_lshlrev_b32_e32 v168, 16, v126
	v_fmac_f32_e32 v164, v173, v168
	v_and_b32_e32 v169, 0xffff0000, v126
	v_fmac_f32_e32 v165, v173, v169
	v_lshlrev_b32_e32 v168, 16, v142
	v_mul_f32_e32 v164, v164, v168
	v_and_b32_e32 v169, 0xffff0000, v142
	v_mul_f32_e32 v165, v165, v169
	v_lshlrev_b32_e32 v168, 16, v127
	v_fmac_f32_e32 v166, v173, v168
	v_and_b32_e32 v169, 0xffff0000, v127
	v_fmac_f32_e32 v167, v173, v169
	v_lshlrev_b32_e32 v168, 16, v143
	v_mul_f32_e32 v166, v166, v168
	v_and_b32_e32 v169, 0xffff0000, v143
	v_mul_f32_e32 v167, v167, v169
	v_cvt_pk_bf16_f32 v196, v160, v161
	v_cvt_pk_bf16_f32 v197, v162, v163
	v_cvt_pk_bf16_f32 v198, v164, v165
	v_cvt_pk_bf16_f32 v199, v166, v167
	global_store_dwordx4 v5, v[196:199], s[12:13] offset:3072
	s_add_i32 s24, s24, 1
	s_cmp_lt_u32 s24, 32
	s_cbranch_scc1 .Lx14_row
	s_waitcnt vmcnt(0)
	s_cmp_lg_u32 s82, 0
	s_cbranch_scc1 .Lx14_fin_other
	s_mov_b32 s27, 0
	v_mov_b32_e32 v5, 0x200
.Lx14_fin0:
	global_load_dword v9, v4, s[20:21] sc1
	global_load_dword v152, v4, s[20:21] offset:128 sc1
	s_waitcnt vmcnt(0)
	ds_write_b32 v4, v9
	ds_write_b32 v4, v152 offset:128
	ds_read_b32 v6, v5
	s_waitcnt lgkmcnt(0)
	v_readfirstlane_b32 s0, v6
	s_cmp_ge_u32 s0, 7
	s_cbranch_scc1 .Lx14_end
	s_sleep 64
	s_add_u32 s27, s27, 1
	s_cmp_lt_u32 s27, 0x4000
	s_cbranch_scc1 .Lx14_fin0
	s_branch .Lx14_end
.Lx14_fin_other:
	v_cmp_eq_u32_e32 vcc, 0, v1
	s_and_saveexec_b64 s[98:99], vcc
	v_mov_b32_e32 v5, 0x200
	v_mov_b32_e32 v6, 1
	ds_add_u32 v5, v6
	s_or_b64 exec, exec, s[98:99]
.Lx14_end:
	s_waitcnt lgkmcnt(0)
.LBB0_1816:
	s_waitcnt lgkmcnt(0)
	s_cmp_gt_i32 s73, 14
	s_cselect_b64 s[6:7], -1, 0
	s_and_b64 s[0:1], s[22:23], s[6:7]
	s_andn2_b64 vcc, exec, s[0:1]
	s_cbranch_vccnz .LBB0_1866
	s_waitcnt vmcnt(0)
	v_cmp_eq_u32_e32 vcc, 0, v0
	s_waitcnt vmcnt(0)
	s_barrier
	s_and_saveexec_b64 s[4:5], vcc
	s_cbranch_execz .LBB0_1865
	s_add_i32 s0, 0, 0x27800
	v_mov_b32_e32 v1, s0
	s_waitcnt vmcnt(0) expcnt(0) lgkmcnt(0)
	ds_read_b32 v3, v1
	s_add_i32 s0, 0, 0x27804
	v_mov_b32_e32 v1, s0
	ds_read_b32 v1, v1
	s_waitcnt lgkmcnt(1)
	v_cmp_ne_u32_e32 vcc, 0, v3
	s_cbranch_vccnz .LBB0_1833
	v_readlane_b32 s8, v255, 0
	v_readlane_b32 s9, v255, 1
	s_load_dwordx2 s[0:1], s[8:9], 0x4
	s_add_u32 s8, s54, 0x1000
	s_addc_u32 s9, s55, 0
	s_add_u32 s10, s54, 0x1100
	s_addc_u32 s11, s55, 0
	s_add_u32 s12, s54, 0x1200
	s_addc_u32 s13, s55, 0
	s_waitcnt lgkmcnt(0)
	s_mul_i32 s3, s0, s33
	s_add_u32 s14, s54, 0x1300
	s_mul_i32 s3, s3, s1
	s_addc_u32 s15, s55, 0
	s_mov_b32 s22, 1
	v_mov_b32_e32 v17, 0
	s_branch .LBB0_1821
